# attention latent units: V tile staged with unswapped key rows so the PV B-operand key order matches the lane halves of P; the 8 v_permlane32_swap per tile that re-ordered packed P are gone
# speedup vs baseline: 1.0046x; 1.0027x over previous
.LBB0_783:
	s_and_b64 vcc, exec, s[0:1]
	s_cbranch_vccz .LBB0_762
	s_ashr_i32 s0, s16, 7
	s_lshl_b32 s18, s0, 11
	s_and_b32 s1, s17, 0x780
	s_or_b32 s17, s18, s1
	s_lshl_b32 s1, s16, 3
	s_and_b32 s1, s1, 0x380
	v_mbcnt_lo_u32_b32 v171, -1, 0
	v_mbcnt_hi_u32_b32 v171, -1, v171
	s_lshl_b32 s96, s1, 1
	v_lshlrev_b32_e32 v20, 3, v171
	v_and_b32_e32 v0, 0x78, v20
	s_add_u32 s20, s6, s96
	v_lshlrev_b32_e32 v16, 1, v0
	s_addc_u32 s21, s7, 0
	v_mov_b32_e32 v17, v113
	v_add_u32_e32 v172, s4, v171
	v_lshl_add_u64 v[166:167], s[20:21], 0, v[16:17]
	s_add_u32 s20, s8, s96
	v_ashrrev_i32_e32 v181, 4, v172
	s_addc_u32 s21, s9, 0
	v_lshl_add_u64 v[168:169], s[20:21], 0, v[16:17]
	v_mad_u32_u24 v241, v181, s62, v16
	v_add_u32_e32 v34, s18, v181
	v_mad_i64_i32 v[0:1], s[20:21], v34, s62, v[168:169]
	v_add_co_u32_e32 v4, vcc, s74, v0
	v_mad_i64_i32 v[8:9], s[20:21], v34, s62, v[166:167]
	s_nop 0
	v_addc_co_u32_e32 v5, vcc, 0, v1, vcc
	v_add_co_u32_e32 v12, vcc, s74, v8
	global_load_dwordx4 v[0:3], v[0:1], off
	s_nop 0
	global_load_dwordx4 v[4:7], v[4:5], off
	v_addc_co_u32_e32 v13, vcc, 0, v9, vcc
	global_load_dwordx4 v[8:11], v[8:9], off
	s_nop 0
	global_load_dwordx4 v[12:15], v[12:13], off
	v_lshrrev_b32_e32 v17, 1, v172
	v_and_b32_e32 v173, 31, v171
	v_and_b32_e32 v176, 0x60, v17
	v_mov_b64_e32 v[18:19], s[50:51]
	v_ashrrev_i32_e32 v175, 8, v172
	v_or3_b32 v29, v173, s17, v176
	v_bfe_u32 v22, v20, 5, 2
	v_lshlrev_b32_e32 v20, 6, v175
	v_mad_i64_i32 v[18:19], s[20:21], v29, s62, v[18:19]
	v_bfe_u32 v174, v171, 5, 1
	v_ashrrev_i32_e32 v21, 31, v20
	v_lshl_add_u64 v[18:19], v[18:19], 0, s[96:97]
	v_lshlrev_b32_e32 v112, 4, v174
	v_lshl_add_u64 v[18:19], v[20:21], 1, v[18:19]
	v_lshl_add_u64 v[18:19], v[18:19], 0, v[112:113]
	global_load_dwordx4 v[122:125], v[18:19], off
	global_load_dwordx4 v[126:129], v[18:19], off offset:32
	global_load_dwordx4 v[118:121], v[18:19], off offset:64
	global_load_dwordx4 v[114:117], v[18:19], off offset:96
	v_and_b32_e32 v17, 0xfffff0, v181
	v_lshlrev_b32_e32 v24, 1, v181
	v_add_u32_e32 v27, 32, v181
	v_lshrrev_b32_e32 v25, 1, v181
	v_and_b32_e32 v26, 3, v181
	v_and_or_b32 v17, v181, 8, v17
	v_and_b32_e32 v20, 0xfffff0, v27
	v_lshlrev_b32_e32 v21, 1, v27
	v_and_b32_e32 v23, 0x70, v172
	v_lshlrev_b32_e32 v28, 8, v181
	v_and_or_b32 v24, v181, 4, v26
	v_lshlrev_b32_e32 v26, 8, v27
	v_lshrrev_b32_e32 v17, 1, v17
	v_and_or_b32 v20, v27, 8, v20
	v_and_b32_e32 v25, 48, v16
	v_bitop3_b32 v182, v16, v28, v23 bitop3:0xde
	v_bitop3_b32 v183, v26, v16, v23 bitop3:0xf6
	v_and_b32_e32 v243, 16, v181
	v_lshlrev_b32_e32 v243, 3, v243
	v_xor_b32_e32 v182, v243, v182
	v_xor_b32_e32 v183, v243, v183
	v_or_b32_e32 v16, v17, v22
	v_lshrrev_b32_e32 v17, 1, v20
	v_lshlrev_b32_e32 v24, 6, v24
	v_lshlrev_b32_e32 v16, 9, v16
	v_or_b32_e32 v17, v17, v22
	v_or3_b32 v184, v16, v24, v25
	v_lshlrev_b32_e32 v16, 9, v17
	v_or3_b32 v185, v16, v24, v25
	v_add_u32_e32 v32, 0, v184
	v_add_u32_e32 v21, 0, v182
	v_add_u32_e32 v20, 0, v183
	v_add_u32_e32 v33, 0, v185
	s_waitcnt vmcnt(0)
	v_lshlrev_b32_e32 v38, 7, v175
	v_lshlrev_b32_e32 v189, 8, v173
	v_add_u32_e32 v191, 0, v189
	s_movk_i32 s1, 0x60
	s_waitcnt vmcnt(7)
	ds_write_b128 v32, v[0:3] offset:1024
	s_waitcnt vmcnt(6)
	ds_write_b128 v33, v[4:7] offset:1024
	s_waitcnt vmcnt(5)
	ds_write_b128 v21, v[8:11] offset:50176
	s_waitcnt vmcnt(4)
	ds_write_b128 v20, v[12:15] offset:50176
	v_add_u32_e32 v4, 64, v34
	v_mad_i64_i32 v[0:1], s[20:21], v4, s62, v[168:169]
	v_add_co_u32_e32 v2, vcc, s74, v0
	s_nop 1
	v_addc_co_u32_e32 v3, vcc, 0, v1, vcc
	global_load_dwordx4 v[16:19], v[0:1], off
	global_load_dwordx4 v[20:23], v[2:3], off
	v_mad_i64_i32 v[0:1], s[20:21], v4, s62, v[166:167]
	v_add_co_u32_e32 v2, vcc, s74, v0
	v_add_u32_e32 v4, 0x80, v34
	s_nop 0
	v_addc_co_u32_e32 v3, vcc, 0, v1, vcc
	global_load_dwordx4 v[24:27], v[0:1], off
	global_load_dwordx4 v[28:31], v[2:3], off
	v_mad_i64_i32 v[0:1], s[20:21], v4, s62, v[166:167]
	v_add_co_u32_e32 v2, vcc, s74, v0
	s_nop 1
	v_addc_co_u32_e32 v3, vcc, 0, v1, vcc
	global_load_dwordx4 v[142:145], v[2:3], off
	global_load_dwordx4 v[138:141], v[0:1], off
	v_mad_i64_i32 v[0:1], s[20:21], v4, s62, v[168:169]
	v_add_co_u32_e32 v2, vcc, s74, v0
	s_nop 1
	v_addc_co_u32_e32 v3, vcc, 0, v1, vcc
	global_load_dwordx4 v[134:137], v[2:3], off
	global_load_dwordx4 v[130:133], v[0:1], off
	v_lshlrev_b32_e32 v0, 4, v171
	v_and_b32_e32 v39, 0x70, v0
	v_bitop3_b32 v190, v38, v39, v112 bitop3:0x36
	v_and_b32_e32 v244, 16, v171
	v_lshlrev_b32_e32 v244, 3, v244
	v_xor_b32_e32 v190, v244, v190
	v_add_u32_e32 v34, v191, v190
	s_waitcnt lgkmcnt(0)
	s_barrier
	ds_read_b128 v[0:3], v34 offset:50176
	ds_read_b128 v[34:37], v34 offset:58368
	v_or_b32_e32 v38, v38, v112
	v_bitop3_b32 v188, v38, v39, 32 bitop3:0x36
	v_xor_b32_e32 v188, v244, v188
	v_add_u32_e32 v40, v191, v188
	s_waitcnt vmcnt(11) lgkmcnt(0)
	v_mfma_f32_32x32x16_bf16 v[64:79], v[34:37], v[122:125], 0
	ds_read_b128 v[34:37], v40 offset:50176
	v_bitop3_b32 v187, v38, v39, 64 bitop3:0x36
	v_bitop3_b32 v186, v38, v39, s1 bitop3:0x36
	v_xor_b32_e32 v187, v244, v187
	v_xor_b32_e32 v186, v244, v186
	v_add_u32_e32 v38, v191, v186
	v_mfma_f32_32x32x16_bf16 v[0:15], v[0:3], v[122:125], 0
	s_waitcnt vmcnt(10) lgkmcnt(0)
	v_mfma_f32_32x32x16_bf16 v[0:15], v[34:37], v[126:129], v[0:15]
	ds_read_b128 v[34:37], v40 offset:58368
	v_add_u32_e32 v40, v191, v187
	s_waitcnt lgkmcnt(0)
	v_mfma_f32_32x32x16_bf16 v[64:79], v[34:37], v[126:129], v[64:79]
	ds_read_b128 v[34:37], v40 offset:50176
	s_waitcnt vmcnt(9) lgkmcnt(0)
	v_mfma_f32_32x32x16_bf16 v[0:15], v[34:37], v[118:121], v[0:15]
	ds_read_b128 v[34:37], v40 offset:58368
	s_waitcnt lgkmcnt(0)
	v_mfma_f32_32x32x16_bf16 v[64:79], v[34:37], v[118:121], v[64:79]
	ds_read_b128 v[34:37], v38 offset:50176
	s_waitcnt vmcnt(8) lgkmcnt(0)
	v_mfma_f32_32x32x16_bf16 v[0:15], v[34:37], v[114:117], v[0:15]
	ds_read_b128 v[34:37], v38 offset:58368
	s_waitcnt lgkmcnt(0)
	v_mfma_f32_32x32x16_bf16 v[64:79], v[34:37], v[114:117], v[64:79]
	s_nop 8
	v_max_f32_e32 v34, v1, v1
	v_max_f32_e32 v35, v0, v0
	v_max_f32_e32 v34, v35, v34
	v_max3_f32 v34, v34, v2, v3
	v_max3_f32 v34, v34, v4, v5
	v_max3_f32 v34, v34, v6, v7
	v_max3_f32 v34, v34, v8, v9
	v_max3_f32 v34, v34, v10, v11
	v_max3_f32 v34, v34, v12, v13
	v_max3_f32 v34, v34, v14, v15
	v_max3_f32 v34, v34, v64, v65
	v_max3_f32 v34, v34, v66, v67
	v_max3_f32 v34, v34, v68, v69
	v_max3_f32 v34, v34, v70, v71
	v_max3_f32 v34, v34, v72, v73
	v_max3_f32 v34, v34, v74, v75
	v_max3_f32 v34, v34, v76, v77
	v_max3_f32 v34, v34, v78, v79
	v_mov_b32_e32 v35, v34
	s_nop 1
	v_permlane32_swap_b32_e32 v34, v35
	v_max_f32_e32 v35, v35, v35
	v_max_f32_e32 v34, v34, v34
	v_max_f32_e32 v34, v34, v35
	v_cmp_ge_f32_e32 vcc, s75, v34
	s_cmp_eq_u64 vcc, exec
	s_cbranch_scc0 .LBB0_814
	v_mov_b32_e32 v193, 1.0
	v_mov_b32_e32 v164, 0

.LBB0_787:
	s_mov_b32 s54, s0
	s_add_i32 s55, s28, -3
	s_lshl_b32 s21, s0, 14
	v_add_u32_e32 v180, s21, v191
	v_add_u32_e32 v84, v180, v190
	ds_read_b128 v[80:83], v84 offset:50176
	ds_read_b128 v[84:87], v84 offset:58368
	v_add_u32_e32 v195, v180, v188
	ds_read_b128 v[196:199], v195 offset:50176
	ds_read_b128 v[200:203], v195 offset:58368
	v_add_u32_e32 v195, v180, v187
	s_waitcnt lgkmcnt(3)
	v_mfma_f32_32x32x16_bf16 v[96:111], v[80:83], v[122:125], 0
	v_add_u32_e32 v180, v180, v186
	v_exp_f32_e32 v204, v72
	v_exp_f32_e32 v205, v73
	v_exp_f32_e32 v206, v74
	v_exp_f32_e32 v207, v75
	v_exp_f32_e32 v208, v76
	v_exp_f32_e32 v209, v77
	s_waitcnt lgkmcnt(2)
	v_mfma_f32_32x32x16_bf16 v[80:95], v[84:87], v[122:125], 0
	v_exp_f32_e32 v210, v78
	v_exp_f32_e32 v79, v79
	s_waitcnt lgkmcnt(1)
	v_mfma_f32_32x32x16_bf16 v[96:111], v[196:199], v[126:129], v[96:111]
	s_waitcnt lgkmcnt(0)
	v_mfma_f32_32x32x16_bf16 v[80:95], v[200:203], v[126:129], v[80:95]
	ds_read_b128 v[196:199], v195 offset:50176
	ds_read_b128 v[200:203], v195 offset:58368
	s_waitcnt lgkmcnt(1)
	v_mfma_f32_32x32x16_bf16 v[96:111], v[196:199], v[118:121], v[96:111]
	s_waitcnt lgkmcnt(0)
	v_mfma_f32_32x32x16_bf16 v[80:95], v[200:203], v[118:121], v[80:95]
	ds_read_b128 v[196:199], v180 offset:50176
	ds_read_b128 v[200:203], v180 offset:58368
	v_exp_f32_e32 v180, v64
	v_add_f32_e32 v64, v161, v159
	v_add_f32_e32 v195, v157, v160
	v_add_f32_e32 v64, v155, v64
	v_add_f32_e32 v195, v158, v195
	v_add_f32_e32 v64, v154, v64
	v_add_f32_e32 v195, v156, v195
	v_add_f32_e32 v64, v151, v64
	v_add_f32_e32 v195, v153, v195
	v_add_f32_e32 v64, v149, v64
	v_add_f32_e32 v195, v152, v195
	v_add_f32_e32 v64, v147, v64
	s_waitcnt lgkmcnt(1)
	v_mfma_f32_32x32x16_bf16 v[96:111], v[196:199], v[114:117], v[96:111]
	v_exp_f32_e32 v197, v65
	v_add_f32_e32 v195, v150, v195
	v_exp_f32_e32 v198, v66
	v_add_f32_e32 v64, v146, v64
	v_exp_f32_e32 v199, v67
	v_add_f32_e32 v195, v148, v195
	v_add_f32_e32 v64, v180, v64
	s_waitcnt lgkmcnt(0)
	v_mfma_f32_32x32x16_bf16 v[80:95], v[200:203], v[114:117], v[80:95]
	v_exp_f32_e32 v200, v68
	v_exp_f32_e32 v201, v69
	v_add_f32_e32 v195, v197, v195
	v_exp_f32_e32 v202, v70
	v_add_f32_e32 v64, v198, v64
	v_exp_f32_e32 v203, v71
	v_add_f32_e32 v195, v199, v195
	v_add_f32_e32 v64, v200, v64
	v_add_f32_e32 v195, v201, v195
	v_add_f32_e32 v64, v202, v64
	v_add_f32_e32 v195, v203, v195
	v_add_f32_e32 v64, v204, v64
	v_add_f32_e32 v195, v205, v195
	v_add_f32_e32 v64, v206, v64
	v_add_f32_e32 v195, v207, v195
	v_add_f32_e32 v64, v208, v64
	v_add_f32_e32 v195, v209, v195
	v_add_f32_e32 v64, v210, v64
	v_add_f32_e32 v195, v79, v195
	v_add_f32_e32 v195, v195, v64
	v_mov_b32_e32 v196, v195
	v_cvt_pk_bf16_f32 v64, v159, v161
	v_cvt_pk_bf16_f32 v65, v157, v160
	v_cvt_pk_bf16_f32 v66, v155, v158
	v_permlane32_swap_b32_e32 v195, v196
	v_cvt_pk_bf16_f32 v67, v154, v156
	v_cvt_pk_bf16_f32 v68, v151, v153
	v_cvt_pk_bf16_f32 v69, v149, v152
	v_cvt_pk_bf16_f32 v70, v147, v150
	v_cvt_pk_bf16_f32 v71, v146, v148
	v_cvt_pk_bf16_f32 v72, v180, v197
	v_cvt_pk_bf16_f32 v73, v198, v199
	v_cvt_pk_bf16_f32 v74, v200, v201
	v_cvt_pk_bf16_f32 v75, v202, v203
	v_cvt_pk_bf16_f32 v76, v204, v205
	v_cvt_pk_bf16_f32 v77, v206, v207
	v_cvt_pk_bf16_f32 v78, v208, v209
	v_cvt_pk_bf16_f32 v79, v210, v79
	s_cmp_lt_u32 s55, 30
	s_cselect_b32 s0, 0, 0xffffffe0
	s_cselect_b32 s1, s18, s16
	s_add_i32 s0, s0, s28
	s_lshl_b32 s0, s0, 6
	s_add_i32 s0, s0, s1
	s_sub_i32 s0, s0, 64
	s_mul_i32 s64, s0, 0x1800
	s_add_u32 s66, s8, s96
	s_addc_u32 s67, s9, 0
	s_add_u32 s66, s66, s64
	s_addc_u32 s67, s67, 0
	s_add_u32 s68, s66, 0x30000
	s_addc_u32 s69, s67, 0
	s_add_u32 s70, s6, s96
	s_addc_u32 s71, s7, 0
	s_add_u32 s70, s70, s64
	s_addc_u32 s71, s71, 0
	s_add_u32 s72, s70, 0x30000
	s_addc_u32 s73, s71, 0
	global_load_dwordx4 v[146:149], v241, s[66:67]
	global_load_dwordx4 v[150:153], v241, s[68:69]
	global_load_dwordx4 v[154:157], v241, s[70:71]
	global_load_dwordx4 v[158:161], v241, s[72:73]
	s_lshl_b32 s20, s29, 14
	v_add_u32_e32 v180, s20, v194
	ds_read_b64_tr_b16 v[198:199], v180 offset:0
	ds_read_b64_tr_b16 v[200:201], v180 offset:0x800
	ds_read_b64_tr_b16 v[202:203], v180 offset:0x1000
	ds_read_b64_tr_b16 v[204:205], v180 offset:0x1800
	ds_read_b64_tr_b16 v[206:207], v180 offset:0x2000
	ds_read_b64_tr_b16 v[208:209], v180 offset:0x2800
	ds_read_b64_tr_b16 v[222:223], v180 offset:0x3000
	ds_read_b64_tr_b16 v[224:225], v180 offset:0x3800
	s_waitcnt lgkmcnt(0)
	s_nop 0
	v_mfma_f32_32x32x16_bf16 v[0:15], v[64:67], v[198:201], v[0:15]
	ds_read_b64_tr_b16 v[198:199], v180 offset:0x200
	ds_read_b64_tr_b16 v[200:201], v180 offset:0xa00
	v_mfma_f32_32x32x16_bf16 v[0:15], v[68:71], v[202:205], v[0:15]
	ds_read_b64_tr_b16 v[202:203], v180 offset:0x1200
	ds_read_b64_tr_b16 v[204:205], v180 offset:0x1a00
	v_mfma_f32_32x32x16_bf16 v[0:15], v[72:75], v[206:209], v[0:15]
	ds_read_b64_tr_b16 v[206:207], v180 offset:0x2200
	ds_read_b64_tr_b16 v[208:209], v180 offset:0x2a00
	v_mfma_f32_32x32x16_bf16 v[0:15], v[76:79], v[222:225], v[0:15]
	ds_read_b64_tr_b16 v[222:223], v180 offset:0x3200
	ds_read_b64_tr_b16 v[224:225], v180 offset:0x3a00
	s_waitcnt lgkmcnt(0)
	v_mfma_f32_32x32x16_bf16 v[48:63], v[64:67], v[198:201], v[48:63]
	ds_read_b64_tr_b16 v[198:199], v180 offset:0x400
	ds_read_b64_tr_b16 v[200:201], v180 offset:0xc00
	v_mfma_f32_32x32x16_bf16 v[48:63], v[68:71], v[202:205], v[48:63]
	ds_read_b64_tr_b16 v[202:203], v180 offset:0x1400
	ds_read_b64_tr_b16 v[204:205], v180 offset:0x1c00
	v_mfma_f32_32x32x16_bf16 v[48:63], v[72:75], v[206:209], v[48:63]
	ds_read_b64_tr_b16 v[206:207], v180 offset:0x2400
	ds_read_b64_tr_b16 v[208:209], v180 offset:0x2c00
	v_mfma_f32_32x32x16_bf16 v[48:63], v[76:79], v[222:225], v[48:63]
	ds_read_b64_tr_b16 v[222:223], v180 offset:0x3400
	ds_read_b64_tr_b16 v[224:225], v180 offset:0x3c00
	s_waitcnt lgkmcnt(0)
	v_mfma_f32_32x32x16_bf16 v[32:47], v[64:67], v[198:201], v[32:47]
	ds_read_b64_tr_b16 v[198:199], v180 offset:0x600
	ds_read_b64_tr_b16 v[200:201], v180 offset:0xe00
	v_mfma_f32_32x32x16_bf16 v[32:47], v[68:71], v[202:205], v[32:47]
	ds_read_b64_tr_b16 v[202:203], v180 offset:0x1600
	ds_read_b64_tr_b16 v[204:205], v180 offset:0x1e00
	v_mfma_f32_32x32x16_bf16 v[32:47], v[72:75], v[206:209], v[32:47]
	ds_read_b64_tr_b16 v[206:207], v180 offset:0x2600
	ds_read_b64_tr_b16 v[208:209], v180 offset:0x2e00
	v_mfma_f32_32x32x16_bf16 v[32:47], v[76:79], v[222:225], v[32:47]
	ds_read_b64_tr_b16 v[222:223], v180 offset:0x3600
	ds_read_b64_tr_b16 v[224:225], v180 offset:0x3e00
	s_waitcnt lgkmcnt(0)
	v_mfma_f32_32x32x16_bf16 v[16:31], v[64:67], v[198:201], v[16:31]
	v_max_f32_e32 v64, v96, v97
	v_max3_f32 v65, v80, v81, v82
	v_max3_f32 v64, v64, v98, v99
	v_max3_f32 v65, v65, v83, v84
	v_max3_f32 v64, v64, v100, v101
	v_mfma_f32_32x32x16_bf16 v[16:31], v[68:71], v[202:205], v[16:31]
	v_max3_f32 v65, v65, v85, v86
	v_max3_f32 v64, v64, v102, v103
	v_max3_f32 v65, v65, v87, v88
	v_max3_f32 v64, v64, v104, v105
	v_max3_f32 v65, v65, v89, v90
	v_max3_f32 v64, v64, v106, v107
	v_max3_f32 v65, v65, v91, v92
	v_mfma_f32_32x32x16_bf16 v[16:31], v[72:75], v[206:209], v[16:31]
	v_max3_f32 v64, v64, v108, v109
	v_max3_f32 v65, v65, v93, v94
	v_max3_f32 v64, v64, v110, v111
	v_max3_f32 v64, v64, v65, v95
	v_mov_b32_e32 v65, v64
	v_cmp_eq_f32_e32 vcc, 0, v164
	v_mov_b32_e32 v198, 1.0
	v_permlane32_swap_b32_e32 v64, v65
	v_mfma_f32_32x32x16_bf16 v[16:31], v[76:79], v[222:225], v[16:31]
	v_max_f32_e32 v64, v64, v65
	v_cmp_ge_f32_e64 s[40:41], s75, v64
	s_and_b64 s[0:1], vcc, s[40:41]
	s_cmp_eq_u64 s[0:1], exec
	s_cbranch_scc0 .LBB0_801

.LBB0_792:
	v_exp_f32_e32 v197, v96
	v_exp_f32_e32 v208, v97
	v_exp_f32_e32 v209, v98
	v_exp_f32_e32 v210, v99
	v_exp_f32_e32 v211, v100
	v_exp_f32_e32 v220, v101
	v_exp_f32_e32 v221, v102
	v_exp_f32_e32 v222, v103
	v_exp_f32_e32 v223, v104
	v_exp_f32_e32 v224, v105
	v_exp_f32_e32 v225, v106
	v_exp_f32_e32 v226, v107
	v_exp_f32_e32 v227, v108
	v_exp_f32_e32 v228, v109
	v_exp_f32_e32 v229, v110
	v_exp_f32_e32 v230, v111
	s_waitcnt lgkmcnt(0)
	s_barrier
	v_add_u32_e32 v199, s22, v189
	v_add_u32_e32 v68, v199, v190
	ds_read_b128 v[64:67], v68 offset:50176
	ds_read_b128 v[68:71], v68 offset:58368
	v_add_u32_e32 v204, v199, v188
	ds_read_b128 v[200:203], v204 offset:50176
	ds_read_b128 v[204:207], v204 offset:58368
	v_exp_f32_e32 v231, v87
	s_waitcnt lgkmcnt(3)
	v_mfma_f32_32x32x16_bf16 v[96:111], v[64:67], v[122:125], 0
	v_exp_f32_e32 v232, v88
	v_exp_f32_e32 v233, v89
	v_exp_f32_e32 v234, v90
	v_exp_f32_e32 v235, v91
	v_exp_f32_e32 v236, v92
	v_exp_f32_e32 v237, v93
	v_exp_f32_e32 v238, v94
	s_waitcnt lgkmcnt(2)
	v_mfma_f32_32x32x16_bf16 v[64:79], v[68:71], v[122:125], 0
	v_exp_f32_e32 v95, v95
	s_waitcnt lgkmcnt(1)
	v_mfma_f32_32x32x16_bf16 v[96:111], v[200:203], v[126:129], v[96:111]
	s_waitcnt lgkmcnt(0)
	v_mfma_f32_32x32x16_bf16 v[64:79], v[204:207], v[126:129], v[64:79]
	v_add_u32_e32 v204, v199, v187
	ds_read_b128 v[200:203], v204 offset:50176
	ds_read_b128 v[204:207], v204 offset:58368
	v_add_u32_e32 v199, v199, v186
	s_waitcnt lgkmcnt(1)
	v_mfma_f32_32x32x16_bf16 v[96:111], v[200:203], v[118:121], v[96:111]
	s_waitcnt lgkmcnt(0)
	v_mfma_f32_32x32x16_bf16 v[64:79], v[204:207], v[118:121], v[64:79]
	ds_read_b128 v[200:203], v199 offset:50176
	ds_read_b128 v[204:207], v199 offset:58368
	s_waitcnt lgkmcnt(1)
	v_mfma_f32_32x32x16_bf16 v[96:111], v[200:203], v[114:117], v[96:111]
	v_exp_f32_e32 v201, v80
	v_add_f32_e32 v80, v208, v197
	v_add_f32_e32 v199, v209, v210
	v_add_f32_e32 v80, v211, v80
	v_add_f32_e32 v199, v220, v199
	v_add_f32_e32 v80, v221, v80
	v_add_f32_e32 v199, v222, v199
	v_add_f32_e32 v80, v223, v80
	v_add_f32_e32 v199, v224, v199
	v_add_f32_e32 v80, v225, v80
	v_add_f32_e32 v199, v226, v199
	v_add_f32_e32 v80, v227, v80
	v_exp_f32_e32 v202, v81
	v_add_f32_e32 v199, v228, v199
	v_exp_f32_e32 v203, v82
	v_add_f32_e32 v80, v229, v80
	s_waitcnt lgkmcnt(0)
	v_mfma_f32_32x32x16_bf16 v[64:79], v[204:207], v[114:117], v[64:79]
	v_exp_f32_e32 v204, v83
	v_add_f32_e32 v199, v230, v199
	v_exp_f32_e32 v205, v84
	v_add_f32_e32 v80, v201, v80
	v_exp_f32_e32 v206, v85
	v_add_f32_e32 v199, v202, v199
	v_exp_f32_e32 v207, v86
	v_add_f32_e32 v80, v203, v80
	v_add_f32_e32 v199, v204, v199
	v_add_f32_e32 v80, v205, v80
	v_add_f32_e32 v199, v206, v199
	v_add_f32_e32 v80, v207, v80
	v_add_f32_e32 v199, v231, v199
	v_add_f32_e32 v80, v232, v80
	v_add_f32_e32 v199, v233, v199
	v_add_f32_e32 v80, v234, v80
	v_add_f32_e32 v199, v235, v199
	v_add_f32_e32 v80, v236, v80
	v_add_f32_e32 v199, v237, v199
	v_add_f32_e32 v80, v238, v80
	v_add_f32_e32 v199, v95, v199
	v_add_f32_e32 v199, v199, v80
	v_mov_b32_e32 v200, v199
	v_cvt_pk_bf16_f32 v80, v197, v208
	v_cvt_pk_bf16_f32 v81, v209, v210
	v_cvt_pk_bf16_f32 v82, v211, v220
	v_cvt_pk_bf16_f32 v83, v221, v222
	v_cvt_pk_bf16_f32 v84, v223, v224
	v_cvt_pk_bf16_f32 v85, v225, v226
	v_cvt_pk_bf16_f32 v86, v227, v228
	v_cvt_pk_bf16_f32 v87, v229, v230
	v_cvt_pk_bf16_f32 v88, v201, v202
	v_cvt_pk_bf16_f32 v89, v203, v204
	v_cvt_pk_bf16_f32 v90, v205, v206
	v_cvt_pk_bf16_f32 v91, v207, v231
	v_cvt_pk_bf16_f32 v92, v232, v233
	v_cvt_pk_bf16_f32 v93, v234, v235
	v_cvt_pk_bf16_f32 v94, v236, v237
	v_cvt_pk_bf16_f32 v95, v238, v95
	v_permlane32_swap_b32_e32 v199, v200
	s_cmp_gt_u32 s55, 32
	s_cbranch_scc1 .LBB0_794
	s_cmp_lt_u32 s55, 29
	s_cselect_b32 s0, 0, 0xffffffe0
	s_cselect_b32 s1, s18, s16
	s_add_i32 s0, s0, s28
	s_lshl_b32 s0, s0, 6
	s_add_i32 s0, s0, s1
	s_mul_i32 s64, s0, 0x1800
	s_add_u32 s66, s8, s96
	s_addc_u32 s67, s9, 0
	s_add_u32 s66, s66, s64
	s_addc_u32 s67, s67, 0
	s_add_u32 s68, s66, 0x30000
	s_addc_u32 s69, s67, 0
	s_add_u32 s70, s6, s96
	s_addc_u32 s71, s7, 0
	s_add_u32 s70, s70, s64
	s_addc_u32 s71, s71, 0
	s_add_u32 s72, s70, 0x30000
	s_addc_u32 s73, s71, 0
	global_load_dwordx4 v[130:133], v241, s[66:67]
	global_load_dwordx4 v[134:137], v241, s[68:69]
	global_load_dwordx4 v[138:141], v241, s[70:71]
	global_load_dwordx4 v[142:145], v241, s[72:73]

.LBB0_803:
	v_add_u32_e32 v134, s20, v189
	v_add_u32_e32 v84, v134, v190
	ds_read_b128 v[80:83], v84 offset:50176
	ds_read_b128 v[84:87], v84 offset:58368
	v_add_u32_e32 v130, v134, v188
	v_exp_f32_e32 v78, v78
	v_exp_f32_e32 v79, v79
	s_waitcnt lgkmcnt(1)
	v_mfma_f32_32x32x16_bf16 v[96:111], v[80:83], v[122:125], 0
	s_waitcnt lgkmcnt(0)
	v_mfma_f32_32x32x16_bf16 v[80:95], v[84:87], v[122:125], 0
	ds_read_b128 v[122:125], v130 offset:50176
	ds_read_b128 v[130:133], v130 offset:58368
	s_waitcnt lgkmcnt(1)
	v_mfma_f32_32x32x16_bf16 v[96:111], v[122:125], v[126:129], v[96:111]
	s_waitcnt lgkmcnt(0)
	v_mfma_f32_32x32x16_bf16 v[80:95], v[130:133], v[126:129], v[80:95]
	v_add_u32_e32 v126, v134, v187
	ds_read_b128 v[122:125], v126 offset:50176
	ds_read_b128 v[126:129], v126 offset:58368
	s_waitcnt lgkmcnt(1)
	v_mfma_f32_32x32x16_bf16 v[96:111], v[122:125], v[118:121], v[96:111]
	v_add_u32_e32 v122, v134, v186
	s_waitcnt lgkmcnt(0)
	v_mfma_f32_32x32x16_bf16 v[80:95], v[126:129], v[118:121], v[80:95]
	ds_read_b128 v[118:121], v122 offset:50176
	ds_read_b128 v[122:125], v122 offset:58368
	v_exp_f32_e32 v126, v76
	v_exp_f32_e32 v127, v77
	s_waitcnt lgkmcnt(1)
	v_mfma_f32_32x32x16_bf16 v[96:111], v[118:121], v[114:117], v[96:111]
	v_exp_f32_e32 v118, v68
	v_exp_f32_e32 v119, v69
	v_exp_f32_e32 v120, v70
	v_exp_f32_e32 v121, v71
	s_waitcnt lgkmcnt(0)
	v_mfma_f32_32x32x16_bf16 v[80:95], v[122:125], v[114:117], v[80:95]
	v_exp_f32_e32 v114, v64
	v_add_f32_e32 v64, 0, v159
	v_add_f32_e32 v64, v161, v64
	v_add_f32_e32 v64, v157, v64
	v_add_f32_e32 v64, v160, v64
	v_add_f32_e32 v64, v155, v64
	v_add_f32_e32 v64, v158, v64
	v_add_f32_e32 v64, v154, v64
	v_add_f32_e32 v64, v156, v64
	v_add_f32_e32 v64, v151, v64
	v_add_f32_e32 v64, v153, v64
	v_add_f32_e32 v64, v149, v64
	v_add_f32_e32 v64, v152, v64
	v_add_f32_e32 v64, v147, v64
	v_exp_f32_e32 v115, v65
	v_add_f32_e32 v64, v150, v64
	v_exp_f32_e32 v116, v66
	v_add_f32_e32 v64, v146, v64
	v_exp_f32_e32 v117, v67
	v_add_f32_e32 v64, v148, v64
	v_add_f32_e32 v64, v114, v64
	v_add_f32_e32 v64, v115, v64
	v_add_f32_e32 v64, v116, v64
	v_add_f32_e32 v64, v117, v64
	v_exp_f32_e32 v122, v72
	v_add_f32_e32 v64, v118, v64
	v_exp_f32_e32 v123, v73
	v_add_f32_e32 v64, v119, v64
	v_exp_f32_e32 v124, v74
	v_add_f32_e32 v64, v120, v64
	v_exp_f32_e32 v125, v75
	v_add_f32_e32 v64, v121, v64
	v_add_f32_e32 v64, v122, v64
	v_add_f32_e32 v64, v123, v64
	v_add_f32_e32 v64, v124, v64
	v_add_f32_e32 v64, v125, v64
	v_add_f32_e32 v64, v126, v64
	v_add_f32_e32 v64, v127, v64
	v_add_f32_e32 v64, v78, v64
	v_add_f32_e32 v64, v79, v64
	v_mov_b32_e32 v65, v64
	v_cvt_pk_bf16_f32 v66, v159, v161
	v_cvt_pk_bf16_f32 v67, v157, v160
	v_cvt_pk_bf16_f32 v68, v155, v158
	v_cvt_pk_bf16_f32 v69, v154, v156
	s_nop 1
	v_permlane32_swap_b32_e32 v64, v65
	v_cvt_pk_bf16_f32 v70, v151, v153
	v_cvt_pk_bf16_f32 v71, v149, v152
	v_cvt_pk_bf16_f32 v72, v147, v150
	v_cvt_pk_bf16_f32 v73, v146, v148
	v_cvt_pk_bf16_f32 v74, v114, v115
	v_cvt_pk_bf16_f32 v75, v116, v117
	v_cvt_pk_bf16_f32 v76, v118, v119
	v_cvt_pk_bf16_f32 v77, v120, v121
	v_cvt_pk_bf16_f32 v114, v122, v123
	v_cvt_pk_bf16_f32 v115, v124, v125
	v_cvt_pk_bf16_f32 v116, v126, v127
	v_cvt_pk_bf16_f32 v117, v78, v79
	s_nop 0
	s_add_i32 s0, 0, 0x4400
	v_add_u32_e32 v78, s0, v192
	ds_read_b64_tr_b16 v[118:119], v78 offset:0
	ds_read_b64_tr_b16 v[120:121], v78 offset:0x800
	ds_read_b64_tr_b16 v[122:123], v78 offset:0x1000
	ds_read_b64_tr_b16 v[124:125], v78 offset:0x1800
	ds_read_b64_tr_b16 v[126:127], v78 offset:0x2000
	ds_read_b64_tr_b16 v[128:129], v78 offset:0x2800
	ds_read_b64_tr_b16 v[130:131], v78 offset:0x3000
	ds_read_b64_tr_b16 v[132:133], v78 offset:0x3800
	s_waitcnt lgkmcnt(0)
	s_nop 0
	v_mfma_f32_32x32x16_bf16 v[0:15], v[66:69], v[118:121], v[0:15]
	ds_read_b64_tr_b16 v[118:119], v78 offset:0x200
	ds_read_b64_tr_b16 v[120:121], v78 offset:0xa00
	v_mfma_f32_32x32x16_bf16 v[0:15], v[70:73], v[122:125], v[0:15]
	ds_read_b64_tr_b16 v[122:123], v78 offset:0x1200
	ds_read_b64_tr_b16 v[124:125], v78 offset:0x1a00
	v_mfma_f32_32x32x16_bf16 v[0:15], v[74:77], v[126:129], v[0:15]
	ds_read_b64_tr_b16 v[126:127], v78 offset:0x2200
	ds_read_b64_tr_b16 v[128:129], v78 offset:0x2a00
	v_mfma_f32_32x32x16_bf16 v[0:15], v[114:117], v[130:133], v[0:15]
	ds_read_b64_tr_b16 v[130:131], v78 offset:0x3200
	ds_read_b64_tr_b16 v[132:133], v78 offset:0x3a00
	s_waitcnt lgkmcnt(0)
	v_mfma_f32_32x32x16_bf16 v[48:63], v[66:69], v[118:121], v[48:63]
	ds_read_b64_tr_b16 v[118:119], v78 offset:0x400
	ds_read_b64_tr_b16 v[120:121], v78 offset:0xc00
	v_mfma_f32_32x32x16_bf16 v[48:63], v[70:73], v[122:125], v[48:63]
	ds_read_b64_tr_b16 v[122:123], v78 offset:0x1400
	ds_read_b64_tr_b16 v[124:125], v78 offset:0x1c00
	v_mfma_f32_32x32x16_bf16 v[48:63], v[74:77], v[126:129], v[48:63]
	ds_read_b64_tr_b16 v[126:127], v78 offset:0x2400
	ds_read_b64_tr_b16 v[128:129], v78 offset:0x2c00
	v_mfma_f32_32x32x16_bf16 v[48:63], v[114:117], v[130:133], v[48:63]
	ds_read_b64_tr_b16 v[130:131], v78 offset:0x3400
	ds_read_b64_tr_b16 v[132:133], v78 offset:0x3c00
	s_waitcnt lgkmcnt(0)
	v_mfma_f32_32x32x16_bf16 v[32:47], v[66:69], v[118:121], v[32:47]
	ds_read_b64_tr_b16 v[118:119], v78 offset:0x600
	ds_read_b64_tr_b16 v[120:121], v78 offset:0xe00
	v_mfma_f32_32x32x16_bf16 v[32:47], v[70:73], v[122:125], v[32:47]
	ds_read_b64_tr_b16 v[122:123], v78 offset:0x1600
	ds_read_b64_tr_b16 v[124:125], v78 offset:0x1e00
	v_mfma_f32_32x32x16_bf16 v[32:47], v[74:77], v[126:129], v[32:47]
	ds_read_b64_tr_b16 v[126:127], v78 offset:0x2600
	ds_read_b64_tr_b16 v[128:129], v78 offset:0x2e00
	v_mfma_f32_32x32x16_bf16 v[32:47], v[114:117], v[130:133], v[32:47]
	ds_read_b64_tr_b16 v[130:131], v78 offset:0x3600
	ds_read_b64_tr_b16 v[132:133], v78 offset:0x3e00
	s_waitcnt lgkmcnt(0)
	v_mfma_f32_32x32x16_bf16 v[16:31], v[66:69], v[118:121], v[16:31]
	v_max_f32_e32 v66, v97, v97
	v_max_f32_e32 v67, v96, v96
	v_max_f32_e32 v66, v67, v66
	v_max3_f32 v66, v66, v98, v99
	v_max3_f32 v66, v66, v100, v101
	v_max3_f32 v66, v66, v102, v103
	v_max3_f32 v66, v66, v104, v105
	v_mfma_f32_32x32x16_bf16 v[16:31], v[70:73], v[122:125], v[16:31]
	v_max3_f32 v66, v66, v106, v107
	v_max3_f32 v66, v66, v108, v109
	v_max3_f32 v66, v66, v110, v111
	v_max3_f32 v66, v66, v80, v81
	v_max3_f32 v66, v66, v82, v83
	v_max3_f32 v66, v66, v84, v85
	v_max3_f32 v66, v66, v86, v87
	v_mfma_f32_32x32x16_bf16 v[16:31], v[74:77], v[126:129], v[16:31]
	v_max3_f32 v66, v66, v88, v89
	v_max3_f32 v66, v66, v90, v91
	v_max3_f32 v66, v66, v92, v93
	v_max3_f32 v66, v66, v94, v95
	v_mov_b32_e32 v67, v66
	s_nop 1
	v_permlane32_swap_b32_e32 v66, v67
	v_mfma_f32_32x32x16_bf16 v[16:31], v[114:117], v[130:133], v[16:31]
	v_max_f32_e32 v67, v67, v67
	v_max_f32_e32 v66, v66, v66
	v_max_f32_e32 v67, v66, v67
	v_cmp_eq_f32_e32 vcc, 0, v164
	v_cmp_ge_f32_e64 s[40:41], s75, v67
	s_and_b64 s[0:1], vcc, s[40:41]
	v_cndmask_b32_e64 v66, 0, 1, s[0:1]
	v_cmp_ne_u32_e32 vcc, 0, v66
	s_cmp_eq_u64 vcc, exec
	v_mov_b32_e32 v66, 1.0
	s_cbranch_scc0 .LBB0_815
	v_cmp_gt_f32_e32 vcc, 1.0, v66
	s_cbranch_vccz .LBB0_808

.LBB0_808:
	v_exp_f32_e32 v69, v96
	v_exp_f32_e32 v70, v97
	v_exp_f32_e32 v71, v98
	v_exp_f32_e32 v72, v99
	v_exp_f32_e32 v73, v100
	v_add_f32_e32 v67, 0, v69
	v_exp_f32_e32 v74, v101
	v_add_f32_e32 v67, v70, v67
	v_exp_f32_e32 v75, v102
	v_add_f32_e32 v67, v71, v67
	v_exp_f32_e32 v76, v103
	v_add_f32_e32 v67, v72, v67
	v_exp_f32_e32 v77, v104
	v_add_f32_e32 v67, v73, v67
	v_exp_f32_e32 v78, v105
	v_add_f32_e32 v67, v74, v67
	v_exp_f32_e32 v79, v106
	v_add_f32_e32 v67, v75, v67
	v_exp_f32_e32 v96, v107
	v_add_f32_e32 v67, v76, v67
	v_exp_f32_e32 v97, v108
	v_add_f32_e32 v67, v77, v67
	v_exp_f32_e32 v98, v109
	v_add_f32_e32 v67, v78, v67
	v_exp_f32_e32 v99, v110
	v_add_f32_e32 v67, v79, v67
	v_exp_f32_e32 v100, v111
	v_add_f32_e32 v67, v96, v67
	v_exp_f32_e32 v80, v80
	v_add_f32_e32 v67, v97, v67
	v_exp_f32_e32 v81, v81
	v_add_f32_e32 v67, v98, v67
	v_exp_f32_e32 v82, v82
	v_add_f32_e32 v67, v99, v67
	v_exp_f32_e32 v83, v83
	v_add_f32_e32 v67, v100, v67
	v_exp_f32_e32 v84, v84
	v_add_f32_e32 v67, v80, v67
	v_exp_f32_e32 v85, v85
	v_add_f32_e32 v67, v81, v67
	v_exp_f32_e32 v86, v86
	v_add_f32_e32 v67, v82, v67
	v_exp_f32_e32 v87, v87
	v_add_f32_e32 v67, v83, v67
	v_exp_f32_e32 v88, v88
	v_add_f32_e32 v67, v84, v67
	v_exp_f32_e32 v89, v89
	v_add_f32_e32 v67, v85, v67
	v_exp_f32_e32 v90, v90
	v_add_f32_e32 v67, v86, v67
	v_exp_f32_e32 v91, v91
	v_add_f32_e32 v67, v87, v67
	v_exp_f32_e32 v92, v92
	v_add_f32_e32 v67, v88, v67
	v_exp_f32_e32 v93, v93
	v_add_f32_e32 v67, v89, v67
	v_exp_f32_e32 v94, v94
	v_add_f32_e32 v67, v90, v67
	v_exp_f32_e32 v95, v95
	v_add_f32_e32 v67, v91, v67
	v_add_f32_e32 v67, v92, v67
	v_add_f32_e32 v67, v93, v67
	v_add_f32_e32 v67, v94, v67
	v_add_f32_e32 v67, v95, v67
	v_mov_b32_e32 v68, v67
	s_nop 1
	v_permlane32_swap_b32_e32 v67, v68
	v_cvt_pk_bf16_f32 v70, v69, v70
	v_cvt_pk_bf16_f32 v71, v71, v72
	v_cvt_pk_bf16_f32 v72, v73, v74
	v_cvt_pk_bf16_f32 v73, v75, v76
	v_cvt_pk_bf16_f32 v74, v77, v78
	v_cvt_pk_bf16_f32 v75, v79, v96
	v_cvt_pk_bf16_f32 v76, v97, v98
	v_cvt_pk_bf16_f32 v77, v99, v100
	v_cvt_pk_bf16_f32 v78, v80, v81
	v_cvt_pk_bf16_f32 v79, v82, v83
	v_cvt_pk_bf16_f32 v80, v84, v85
	v_cvt_pk_bf16_f32 v81, v86, v87
	v_cvt_pk_bf16_f32 v82, v88, v89
	v_cvt_pk_bf16_f32 v83, v90, v91
	v_cvt_pk_bf16_f32 v84, v92, v93
	v_cvt_pk_bf16_f32 v85, v94, v95
	s_nop 0
	ds_read_b64_tr_b16 v[86:87], v180 offset:0
	ds_read_b64_tr_b16 v[88:89], v180 offset:0x800
	ds_read_b64_tr_b16 v[90:91], v180 offset:0x1000
	ds_read_b64_tr_b16 v[92:93], v180 offset:0x1800
	ds_read_b64_tr_b16 v[94:95], v180 offset:0x2000
	ds_read_b64_tr_b16 v[96:97], v180 offset:0x2800
	ds_read_b64_tr_b16 v[98:99], v180 offset:0x3000
	ds_read_b64_tr_b16 v[100:101], v180 offset:0x3800
	s_waitcnt lgkmcnt(0)
	s_nop 0
	v_mfma_f32_32x32x16_bf16 v[0:15], v[70:73], v[86:89], v[0:15]
	ds_read_b64_tr_b16 v[86:87], v180 offset:0x200
	ds_read_b64_tr_b16 v[88:89], v180 offset:0xa00
	v_mfma_f32_32x32x16_bf16 v[0:15], v[74:77], v[90:93], v[0:15]
	ds_read_b64_tr_b16 v[90:91], v180 offset:0x1200
	ds_read_b64_tr_b16 v[92:93], v180 offset:0x1a00
	v_mfma_f32_32x32x16_bf16 v[0:15], v[78:81], v[94:97], v[0:15]
	ds_read_b64_tr_b16 v[94:95], v180 offset:0x2200
	ds_read_b64_tr_b16 v[96:97], v180 offset:0x2a00
	v_mfma_f32_32x32x16_bf16 v[0:15], v[82:85], v[98:101], v[0:15]
	ds_read_b64_tr_b16 v[98:99], v180 offset:0x3200
	ds_read_b64_tr_b16 v[100:101], v180 offset:0x3a00
	s_waitcnt lgkmcnt(0)
	v_mfma_f32_32x32x16_bf16 v[48:63], v[70:73], v[86:89], v[48:63]
	ds_read_b64_tr_b16 v[86:87], v180 offset:0x400
	ds_read_b64_tr_b16 v[88:89], v180 offset:0xc00
	v_mfma_f32_32x32x16_bf16 v[48:63], v[74:77], v[90:93], v[48:63]
	ds_read_b64_tr_b16 v[90:91], v180 offset:0x1400
	ds_read_b64_tr_b16 v[92:93], v180 offset:0x1c00
	v_mfma_f32_32x32x16_bf16 v[48:63], v[78:81], v[94:97], v[48:63]
	ds_read_b64_tr_b16 v[94:95], v180 offset:0x2400
	ds_read_b64_tr_b16 v[96:97], v180 offset:0x2c00
	v_mfma_f32_32x32x16_bf16 v[48:63], v[82:85], v[98:101], v[48:63]
	ds_read_b64_tr_b16 v[98:99], v180 offset:0x3400
	ds_read_b64_tr_b16 v[100:101], v180 offset:0x3c00
	s_waitcnt lgkmcnt(0)
	v_mfma_f32_32x32x16_bf16 v[32:47], v[70:73], v[86:89], v[32:47]
	ds_read_b64_tr_b16 v[86:87], v180 offset:0x600
	ds_read_b64_tr_b16 v[88:89], v180 offset:0xe00
	v_mfma_f32_32x32x16_bf16 v[32:47], v[74:77], v[90:93], v[32:47]
	ds_read_b64_tr_b16 v[90:91], v180 offset:0x1600
	ds_read_b64_tr_b16 v[92:93], v180 offset:0x1e00
	v_mfma_f32_32x32x16_bf16 v[32:47], v[78:81], v[94:97], v[32:47]
	ds_read_b64_tr_b16 v[94:95], v180 offset:0x2600
	ds_read_b64_tr_b16 v[96:97], v180 offset:0x2e00
	v_mfma_f32_32x32x16_bf16 v[32:47], v[82:85], v[98:101], v[32:47]
	ds_read_b64_tr_b16 v[98:99], v180 offset:0x3600
	ds_read_b64_tr_b16 v[100:101], v180 offset:0x3e00
	s_waitcnt lgkmcnt(0)
	v_mfma_f32_32x32x16_bf16 v[16:31], v[70:73], v[86:89], v[16:31]
	v_mfma_f32_32x32x16_bf16 v[16:31], v[74:77], v[90:93], v[16:31]
	v_mfma_f32_32x32x16_bf16 v[16:31], v[78:81], v[94:97], v[16:31]
	v_mfma_f32_32x32x16_bf16 v[16:31], v[82:85], v[98:101], v[16:31]
	s_and_saveexec_b64 s[0:1], s[38:39]
	s_cbranch_execz .LBB0_761
	v_add_f32_e32 v64, v64, v65
	v_fmac_f32_e32 v64, v179, v197
	v_add_f32_e32 v65, v67, v68
	v_fmac_f32_e32 v65, v64, v66
	ds_write_b32 v178, v65
	s_branch .LBB0_761
